# ssd_out epilogues: group-norm weight loads issued before the ssq barrier instead of after it (latency hidden behind the barrier wait)
# baseline (speedup 1.0000x reference)
.LBB0_1237:
	s_or_b64 exec, exec, s[0:1]
	v_lshl_add_u64 v[0:1], s[14:15], 2, v[170:171]
	s_nop 0
	global_load_dwordx4 v[12:15], v[0:1], off
	global_load_dwordx4 v[8:11], v[0:1], off offset:64
	global_load_dwordx4 v[4:7], v[0:1], off offset:128
	s_nop 0
	global_load_dwordx4 v[0:3], v[0:1], off offset:192
	s_waitcnt lgkmcnt(0)
	s_waitcnt lgkmcnt(0)
	s_barrier
	v_or_b32_e32 v242, s55, v167
	v_and_b32_e32 v243, 7, v219
	v_lshlrev_b32_e32 v243, 4, v243
	s_lshl_b32 s100, s14, 1
	v_lshl_add_u32 v242, v242, 13, v243
	v_add_u32_e32 v244, v209, v160
	v_add_u32_e32 v242, s100, v242
	v_add_u32_e32 v245, v211, v160
	v_add_u32_e32 v246, v212, v160
	v_add_u32_e32 v247, v210, v160
	v_lshl_add_u32 v116, v166, 2, s16
	ds_read2_b32 v[96:97], v116 offset1:16
	ds_read2_b32 v[98:99], v116 offset0:64 offset1:80
	ds_read2_b32 v[100:101], v116 offset0:128 offset1:144
	ds_read2_b32 v[102:103], v116 offset0:192 offset1:208
	v_add_u32_e32 v117, 0x400, v116
	s_waitcnt lgkmcnt(3)
	v_mov_b32_e32 v114, v97
	v_mov_b32_e32 v115, v96
	s_waitcnt lgkmcnt(2)
	v_mov_b32_e32 v96, v99
	v_mov_b32_e32 v97, v98
	s_waitcnt lgkmcnt(1)
	v_mov_b32_e32 v98, v101
	v_mov_b32_e32 v99, v100
	s_waitcnt lgkmcnt(0)
	v_mov_b32_e32 v100, v103
	v_mov_b32_e32 v101, v102
	v_pk_add_f32 v[102:103], v[114:115], 0 op_sel_hi:[1,0]
	ds_read2_b32 v[106:107], v117 offset1:16
	ds_read2_b32 v[108:109], v117 offset0:64 offset1:80
	ds_read2_b32 v[110:111], v117 offset0:128 offset1:144
	ds_read2_b32 v[112:113], v117 offset0:192 offset1:208
	v_pk_add_f32 v[96:97], v[102:103], v[96:97]
	s_waitcnt lgkmcnt(3)
	v_mov_b32_e32 v114, v107
	v_pk_add_f32 v[96:97], v[96:97], v[98:99]
	v_mov_b32_e32 v115, v106
	v_pk_add_f32 v[96:97], v[96:97], v[100:101]
	s_waitcnt lgkmcnt(2)
	v_mov_b32_e32 v106, v109
	v_mov_b32_e32 v107, v108
	v_pk_add_f32 v[96:97], v[96:97], v[114:115]
	s_waitcnt lgkmcnt(1)
	v_mov_b32_e32 v108, v111
	v_mov_b32_e32 v109, v110
	v_pk_add_f32 v[96:97], v[96:97], v[106:107]
	s_mov_b32 s0, 0x358637bd
	s_waitcnt lgkmcnt(0)
	v_mov_b32_e32 v110, v113
	v_mov_b32_e32 v111, v112
	v_pk_add_f32 v[96:97], v[96:97], v[108:109]
	v_mov_b64_e32 v[80:81], s[0:1]
	v_pk_add_f32 v[96:97], v[96:97], v[110:111]
	s_mov_b32 s16, 0x3b000000
	v_or_b32_e32 v78, s14, v162
	v_pk_fma_f32 v[96:97], v[96:97], s[16:17], v[80:81] op_sel_hi:[1,0,0]
	s_mov_b32 s14, 0x800000
	v_mul_f32_e32 v32, 0x4b800000, v97
	v_cmp_gt_f32_e64 s[0:1], s14, v97
	v_ashrrev_i32_e32 v175, 31, v174
	v_lshlrev_b64 v[104:105], 13, v[174:175]
	v_cndmask_b32_e64 v32, v97, v32, s[0:1]
	v_rsq_f32_e32 v32, v32
	v_ashrrev_i32_e32 v79, 31, v78
	v_lshl_add_u64 v[98:99], s[10:11], 0, v[104:105]
	v_lshlrev_b64 v[78:79], 1, v[78:79]
	v_mul_f32_e32 v97, 0x45800000, v32
	v_cndmask_b32_e64 v32, v32, v97, s[0:1]
	v_pk_mul_f32 v[66:67], v[66:67], v[32:33] op_sel_hi:[1,0]
	v_pk_mul_f32 v[68:69], v[68:69], v[32:33] op_sel_hi:[1,0]
	v_pk_mul_f32 v[62:63], v[62:63], v[32:33] op_sel_hi:[1,0]
	v_pk_mul_f32 v[64:65], v[64:65], v[32:33] op_sel_hi:[1,0]
	v_pk_mul_f32 v[58:59], v[58:59], v[32:33] op_sel_hi:[1,0]
	v_pk_mul_f32 v[60:61], v[60:61], v[32:33] op_sel_hi:[1,0]
	v_pk_mul_f32 v[72:73], v[72:73], v[32:33] op_sel_hi:[1,0]
	v_pk_mul_f32 v[56:57], v[56:57], v[32:33] op_sel_hi:[1,0]
	v_mul_f32_e32 v32, 0x4b800000, v96
	v_cmp_gt_f32_e64 s[0:1], s14, v96
	v_lshl_add_u64 v[98:99], v[98:99], 0, v[78:79]
	v_ashrrev_i32_e32 v55, 31, v54
	v_cndmask_b32_e64 v32, v96, v32, s[0:1]
	v_rsq_f32_e32 v32, v32
	v_lshlrev_b64 v[54:55], 13, v[54:55]
	v_lshl_add_u64 v[54:55], s[10:11], 0, v[54:55]
	v_ashrrev_i32_e32 v77, 31, v76
	v_ashrrev_i32_e32 v75, 31, v74
	s_add_i32 s54, s54, s94
	s_xor_b32 s33, s33, 1
	s_cmpk_lt_i32 s54, 0x400
	s_waitcnt vmcnt(3)
	v_pk_mul_f32 v[68:69], v[14:15], v[68:69]
	v_pk_mul_f32 v[66:67], v[12:13], v[66:67]
	s_waitcnt vmcnt(1)
	v_pk_mul_f32 v[60:61], v[6:7], v[60:61]
	v_pk_mul_f32 v[58:59], v[4:5], v[58:59]
	v_pk_mul_f32 v[64:65], v[10:11], v[64:65]
	v_pk_mul_f32 v[62:63], v[8:9], v[62:63]
	v_cvt_pk_bf16_f32 v66, v66, v67
	v_cvt_pk_bf16_f32 v67, v68, v69
	v_cvt_pk_bf16_f32 v58, v58, v59
	v_cvt_pk_bf16_f32 v59, v60, v61
	v_cvt_pk_bf16_f32 v62, v62, v63
	v_cvt_pk_bf16_f32 v63, v64, v65
	ds_write_b64 v244, v[66:67]
	ds_write_b64 v244, v[62:63] offset:32
	ds_write_b64 v244, v[58:59] offset:64
	s_waitcnt vmcnt(0)
	v_pk_mul_f32 v[56:57], v[2:3], v[56:57]
	v_pk_mul_f32 v[58:59], v[0:1], v[72:73]
	s_nop 0
	v_cvt_pk_bf16_f32 v58, v58, v59
	v_cvt_pk_bf16_f32 v59, v56, v57
	v_mul_f32_e32 v56, 0x45800000, v32
	v_cndmask_b32_e64 v32, v32, v56, s[0:1]
	v_pk_mul_f32 v[50:51], v[50:51], v[32:33] op_sel_hi:[1,0]
	v_pk_mul_f32 v[52:53], v[52:53], v[32:33] op_sel_hi:[1,0]
	v_pk_mul_f32 v[46:47], v[46:47], v[32:33] op_sel_hi:[1,0]
	v_pk_mul_f32 v[48:49], v[48:49], v[32:33] op_sel_hi:[1,0]
	v_pk_mul_f32 v[42:43], v[42:43], v[32:33] op_sel_hi:[1,0]
	v_pk_mul_f32 v[44:45], v[44:45], v[32:33] op_sel_hi:[1,0]
	v_pk_mul_f32 v[28:29], v[28:29], v[32:33] op_sel_hi:[1,0]
	v_pk_mul_f32 v[30:31], v[30:31], v[32:33] op_sel_hi:[1,0]
	v_pk_mul_f32 v[52:53], v[14:15], v[52:53]
	v_pk_mul_f32 v[50:51], v[12:13], v[50:51]
	v_pk_mul_f32 v[48:49], v[10:11], v[48:49]
	v_pk_mul_f32 v[46:47], v[8:9], v[46:47]
	v_pk_mul_f32 v[44:45], v[6:7], v[44:45]
	v_pk_mul_f32 v[42:43], v[4:5], v[42:43]
	v_pk_mul_f32 v[30:31], v[2:3], v[30:31]
	v_pk_mul_f32 v[28:29], v[0:1], v[28:29]
	v_cvt_pk_bf16_f32 v50, v50, v51
	v_cvt_pk_bf16_f32 v51, v52, v53
	v_lshl_add_u64 v[52:53], v[54:55], 0, v[78:79]
	v_cvt_pk_bf16_f32 v46, v46, v47
	v_cvt_pk_bf16_f32 v47, v48, v49
	v_cvt_pk_bf16_f32 v42, v42, v43
	v_cvt_pk_bf16_f32 v43, v44, v45
	v_cvt_pk_bf16_f32 v28, v28, v29
	v_cvt_pk_bf16_f32 v29, v30, v31
	ds_write_b64 v244, v[58:59] offset:96
	ds_write_b64 v245, v[50:51]
	ds_write_b64 v245, v[46:47] offset:32
	ds_write_b64 v245, v[42:43] offset:64
	ds_write_b64 v245, v[28:29] offset:96
	ds_read2_b32 v[28:29], v116 offset0:32 offset1:48
	ds_read2_b32 v[30:31], v116 offset0:96 offset1:112
	ds_read2_b32 v[42:43], v116 offset0:160 offset1:176
	ds_read2_b32 v[44:45], v116 offset0:224 offset1:240
	ds_read2_b32 v[46:47], v117 offset0:32 offset1:48
	ds_read2_b32 v[48:49], v117 offset0:96 offset1:112
	ds_read2_b32 v[50:51], v117 offset0:160 offset1:176
	ds_read2_b32 v[52:53], v117 offset0:224 offset1:240
	s_waitcnt lgkmcnt(7)
	v_mov_b32_e32 v54, v29
	v_mov_b32_e32 v55, v28
	v_pk_add_f32 v[28:29], v[54:55], 0 op_sel_hi:[1,0]
	s_waitcnt lgkmcnt(6)
	v_mov_b32_e32 v54, v31
	v_mov_b32_e32 v55, v30
	v_pk_add_f32 v[28:29], v[28:29], v[54:55]
	s_waitcnt lgkmcnt(5)
	v_mov_b32_e32 v30, v43
	v_mov_b32_e32 v31, v42
	v_pk_add_f32 v[28:29], v[28:29], v[30:31]
	s_waitcnt lgkmcnt(4)
	v_mov_b32_e32 v30, v45
	v_mov_b32_e32 v31, v44
	v_pk_add_f32 v[28:29], v[28:29], v[30:31]
	s_waitcnt lgkmcnt(3)
	v_mov_b32_e32 v30, v47
	v_mov_b32_e32 v31, v46
	v_pk_add_f32 v[28:29], v[28:29], v[30:31]
	s_waitcnt lgkmcnt(2)
	v_mov_b32_e32 v30, v49
	v_mov_b32_e32 v31, v48
	v_pk_add_f32 v[28:29], v[28:29], v[30:31]
	s_waitcnt lgkmcnt(1)
	v_mov_b32_e32 v30, v51
	v_mov_b32_e32 v31, v50
	v_pk_add_f32 v[28:29], v[28:29], v[30:31]
	s_waitcnt lgkmcnt(0)
	v_mov_b32_e32 v30, v53
	v_mov_b32_e32 v31, v52
	v_pk_add_f32 v[28:29], v[28:29], v[30:31]
	s_nop 0
	v_pk_fma_f32 v[28:29], v[28:29], s[16:17], v[80:81] op_sel_hi:[1,0,0]
	s_nop 0
	v_mul_f32_e32 v30, 0x4b800000, v29
	v_cmp_gt_f32_e64 s[0:1], s14, v29
	s_nop 1
	v_cndmask_b32_e64 v29, v29, v30, s[0:1]
	v_rsq_f32_e32 v29, v29
	v_lshlrev_b64 v[30:31], 13, v[76:77]
	v_lshl_add_u64 v[30:31], s[10:11], 0, v[30:31]
	v_lshl_add_u64 v[30:31], v[30:31], 0, v[78:79]
	v_mul_f32_e32 v32, 0x45800000, v29
	v_cndmask_b32_e64 v32, v29, v32, s[0:1]
	v_pk_mul_f32 v[20:21], v[20:21], v[32:33] op_sel_hi:[1,0]
	v_pk_mul_f32 v[22:23], v[22:23], v[32:33] op_sel_hi:[1,0]
	v_pk_mul_f32 v[20:21], v[8:9], v[20:21]
	v_pk_mul_f32 v[22:23], v[10:11], v[22:23]
	v_cvt_pk_bf16_f32 v20, v20, v21
	v_cvt_pk_bf16_f32 v21, v22, v23
	ds_write_b64 v246, v[20:21] offset:32
	v_pk_mul_f32 v[16:17], v[16:17], v[32:33] op_sel_hi:[1,0]
	v_pk_mul_f32 v[18:19], v[18:19], v[32:33] op_sel_hi:[1,0]
	v_mul_f32_e32 v20, 0x4b800000, v28
	v_cmp_gt_f32_e64 s[0:1], s14, v28
	v_pk_mul_f32 v[18:19], v[6:7], v[18:19]
	v_pk_mul_f32 v[16:17], v[4:5], v[16:17]
	v_cndmask_b32_e64 v20, v28, v20, s[0:1]
	v_cvt_pk_bf16_f32 v16, v16, v17
	v_cvt_pk_bf16_f32 v17, v18, v19
	v_rsq_f32_e32 v20, v20
	ds_write_b64 v246, v[16:17] offset:64
	v_pk_mul_f32 v[16:17], v[24:25], v[32:33] op_sel_hi:[1,0]
	v_pk_mul_f32 v[18:19], v[26:27], v[32:33] op_sel_hi:[1,0]
	v_pk_mul_f32 v[16:17], v[0:1], v[16:17]
	v_pk_mul_f32 v[18:19], v[2:3], v[18:19]
	v_cvt_pk_bf16_f32 v16, v16, v17
	v_cvt_pk_bf16_f32 v17, v18, v19
	ds_write_b64 v246, v[16:17] offset:96
	v_mul_f32_e32 v16, 0x45800000, v20
	v_cndmask_b32_e64 v16, v20, v16, s[0:1]
	v_pk_mul_f32 v[38:39], v[38:39], v[32:33] op_sel_hi:[1,0]
	v_pk_mul_f32 v[40:41], v[40:41], v[32:33] op_sel_hi:[1,0]
	v_lshlrev_b64 v[18:19], 13, v[74:75]
	v_pk_mul_f32 v[20:21], v[94:95], v[16:17] op_sel_hi:[1,0]
	v_pk_mul_f32 v[22:23], v[90:91], v[16:17] op_sel_hi:[1,0]
	v_pk_mul_f32 v[40:41], v[14:15], v[40:41]
	v_pk_mul_f32 v[38:39], v[12:13], v[38:39]
	v_lshl_add_u64 v[18:19], s[10:11], 0, v[18:19]
	v_pk_mul_f32 v[14:15], v[14:15], v[22:23]
	v_pk_mul_f32 v[12:13], v[12:13], v[20:21]
	v_cvt_pk_bf16_f32 v38, v38, v39
	v_cvt_pk_bf16_f32 v12, v12, v13
	v_cvt_pk_bf16_f32 v13, v14, v15
	v_lshl_add_u64 v[14:15], v[18:19], 0, v[78:79]
	ds_write_b64 v247, v[12:13]
	v_pk_mul_f32 v[12:13], v[92:93], v[16:17] op_sel_hi:[1,0]
	v_pk_mul_f32 v[18:19], v[86:87], v[16:17] op_sel_hi:[1,0]
	v_pk_mul_f32 v[8:9], v[8:9], v[12:13]
	v_pk_mul_f32 v[10:11], v[10:11], v[18:19]
	v_cvt_pk_bf16_f32 v8, v8, v9
	v_cvt_pk_bf16_f32 v9, v10, v11
	ds_write_b64 v247, v[8:9] offset:32
	v_pk_mul_f32 v[8:9], v[88:89], v[16:17] op_sel_hi:[1,0]
	v_pk_mul_f32 v[10:11], v[82:83], v[16:17] op_sel_hi:[1,0]
	v_pk_mul_f32 v[4:5], v[4:5], v[8:9]
	v_pk_mul_f32 v[6:7], v[6:7], v[10:11]
	v_cvt_pk_bf16_f32 v4, v4, v5
	v_cvt_pk_bf16_f32 v5, v6, v7
	ds_write_b64 v247, v[4:5] offset:64
	v_pk_mul_f32 v[4:5], v[84:85], v[16:17] op_sel_hi:[1,0]
	v_pk_mul_f32 v[6:7], v[70:71], v[16:17] op_sel_hi:[1,0]
	v_pk_mul_f32 v[0:1], v[0:1], v[4:5]
	v_pk_mul_f32 v[2:3], v[2:3], v[6:7]
	v_cvt_pk_bf16_f32 v39, v40, v41
	v_cvt_pk_bf16_f32 v0, v0, v1
	v_cvt_pk_bf16_f32 v1, v2, v3
	ds_write_b64 v246, v[38:39]
	ds_write_b64 v247, v[0:1] offset:96
	s_waitcnt lgkmcnt(0)
	ds_read_b128 v[0:3], v213
	ds_read_b128 v[4:7], v213 offset:1280
	ds_read_b128 v[8:11], v213 offset:2560
	ds_read_b128 v[12:15], v213 offset:3840
	ds_read_b128 v[16:19], v213 offset:5120
	ds_read_b128 v[20:23], v213 offset:6400
	ds_read_b128 v[24:27], v213 offset:7680
	ds_read_b128 v[28:31], v213 offset:8960
	s_waitcnt lgkmcnt(7)
	global_store_dwordx4 v242, v[0:3], s[10:11]
	v_add_u32_e32 v242, 0x10000, v242
	s_waitcnt lgkmcnt(6)
	global_store_dwordx4 v242, v[4:7], s[10:11]
	v_add_u32_e32 v242, 0x10000, v242
	s_waitcnt lgkmcnt(5)
	global_store_dwordx4 v242, v[8:11], s[10:11]
	v_add_u32_e32 v242, 0x10000, v242
	s_waitcnt lgkmcnt(4)
	global_store_dwordx4 v242, v[12:15], s[10:11]
	v_add_u32_e32 v242, 0x10000, v242
	s_waitcnt lgkmcnt(3)
	global_store_dwordx4 v242, v[16:19], s[10:11]
	v_add_u32_e32 v242, 0x10000, v242
	s_waitcnt lgkmcnt(2)
	global_store_dwordx4 v242, v[20:23], s[10:11]
	v_add_u32_e32 v242, 0x10000, v242
	s_waitcnt lgkmcnt(1)
	global_store_dwordx4 v242, v[24:27], s[10:11]
	v_add_u32_e32 v242, 0x10000, v242
	s_waitcnt lgkmcnt(0)
	global_store_dwordx4 v242, v[28:31], s[10:11]
	s_nop 1
	s_cbranch_scc0 .LBB0_1246

.LBB0_1267:
	s_or_b64 exec, exec, s[0:1]
	v_lshl_add_u64 v[0:1], s[12:13], 2, v[164:165]
	s_nop 0
	global_load_dwordx4 v[12:15], v[0:1], off
	global_load_dwordx4 v[8:11], v[0:1], off offset:64
	global_load_dwordx4 v[4:7], v[0:1], off offset:128
	s_nop 0
	global_load_dwordx4 v[0:3], v[0:1], off offset:192
	s_waitcnt lgkmcnt(0)
	s_waitcnt lgkmcnt(0)
	s_barrier
	v_lshrrev_b32_e32 v243, 2, v169
	v_and_b32_e32 v242, 3, v219
	v_or_b32_e32 v244, s28, v243
	v_sub_u32_e32 v243, v243, v166
	v_lshlrev_b32_e32 v242, 4, v242
	v_mul_i32_i24_e32 v243, 0xa0, v243
	v_lshl_add_u32 v244, v244, 12, v242
	v_add_u32_e32 v243, v243, v192
	v_add_u32_e32 v244, s12, v244
	v_add_u32_e32 v243, v243, v242
	v_add_u32_e32 v245, v192, v170
	v_add_u32_e32 v246, v197, v170
	v_add_u32_e32 v247, v209, v170
	v_add_u32_e32 v242, v211, v170
	v_lshl_add_u32 v116, v166, 2, s14
	ds_read2_b32 v[96:97], v116 offset1:16
	ds_read2_b32 v[98:99], v116 offset0:64 offset1:80
	ds_read2_b32 v[100:101], v116 offset0:128 offset1:144
	ds_read2_b32 v[102:103], v116 offset0:192 offset1:208
	v_add_u32_e32 v121, 0x400, v116
	s_waitcnt lgkmcnt(3)
	v_mov_b32_e32 v114, v97
	v_mov_b32_e32 v115, v96
	s_waitcnt lgkmcnt(2)
	v_mov_b32_e32 v96, v99
	v_mov_b32_e32 v97, v98
	s_waitcnt lgkmcnt(1)
	v_mov_b32_e32 v98, v101
	v_mov_b32_e32 v99, v100
	s_waitcnt lgkmcnt(0)
	v_mov_b32_e32 v100, v103
	v_mov_b32_e32 v101, v102
	v_pk_add_f32 v[102:103], v[114:115], 0 op_sel_hi:[1,0]
	ds_read2_b32 v[106:107], v121 offset1:16
	ds_read2_b32 v[108:109], v121 offset0:64 offset1:80
	ds_read2_b32 v[110:111], v121 offset0:128 offset1:144
	ds_read2_b32 v[112:113], v121 offset0:192 offset1:208
	v_pk_add_f32 v[96:97], v[102:103], v[96:97]
	s_waitcnt lgkmcnt(3)
	v_mov_b32_e32 v114, v107
	v_pk_add_f32 v[96:97], v[96:97], v[98:99]
	v_mov_b32_e32 v115, v106
	v_pk_add_f32 v[96:97], v[96:97], v[100:101]
	s_waitcnt lgkmcnt(2)
	v_mov_b32_e32 v106, v109
	v_mov_b32_e32 v107, v108
	v_pk_add_f32 v[96:97], v[96:97], v[114:115]
	s_waitcnt lgkmcnt(1)
	v_mov_b32_e32 v108, v111
	v_mov_b32_e32 v109, v110
	v_pk_add_f32 v[96:97], v[96:97], v[106:107]
	s_mov_b32 s0, 0x358637bd
	s_waitcnt lgkmcnt(0)
	v_mov_b32_e32 v110, v113
	v_mov_b32_e32 v111, v112
	v_pk_add_f32 v[96:97], v[96:97], v[108:109]
	v_mov_b64_e32 v[80:81], s[0:1]
	v_pk_add_f32 v[96:97], v[96:97], v[110:111]
	s_mov_b32 s14, 0x3b000000
	v_or_b32_e32 v78, s12, v170
	v_pk_fma_f32 v[96:97], v[96:97], s[14:15], v[80:81] op_sel_hi:[1,0,0]
	s_mov_b32 s12, 0x800000
	v_mul_f32_e32 v32, 0x4b800000, v97
	v_cmp_gt_f32_e64 s[0:1], s12, v97
	v_mov_b32_e32 v120, v33
	v_mov_b32_e32 v117, v33
	v_cndmask_b32_e64 v32, v97, v32, s[0:1]
	v_rsq_f32_e32 v32, v32
	v_mul_f32_e32 v97, 0x4b800000, v96
	v_mov_b32_e32 v118, v33
	v_mov_b32_e32 v119, v33
	v_mul_f32_e32 v100, 0x45800000, v32
	v_cndmask_b32_e64 v32, v32, v100, s[0:1]
	v_pk_mul_f32 v[72:73], v[72:73], v[32:33] op_sel_hi:[1,0]
	v_cmp_gt_f32_e64 s[0:1], s12, v96
	v_pk_mul_f32 v[66:67], v[66:67], v[32:33] op_sel_hi:[1,0]
	v_pk_mul_f32 v[68:69], v[68:69], v[32:33] op_sel_hi:[1,0]
	v_pk_mul_f32 v[62:63], v[62:63], v[32:33] op_sel_hi:[1,0]
	v_pk_mul_f32 v[64:65], v[64:65], v[32:33] op_sel_hi:[1,0]
	v_pk_mul_f32 v[58:59], v[58:59], v[32:33] op_sel_hi:[1,0]
	v_pk_mul_f32 v[60:61], v[60:61], v[32:33] op_sel_hi:[1,0]
	v_pk_mul_f32 v[56:57], v[56:57], v[32:33] op_sel_hi:[1,0]
	v_cndmask_b32_e64 v32, v96, v97, s[0:1]
	v_rsq_f32_e32 v32, v32
	v_ashrrev_i32_e32 v173, 31, v172
	v_ashrrev_i32_e32 v55, 31, v54
	v_lshlrev_b64 v[104:105], 12, v[172:173]
	v_lshlrev_b64 v[54:55], 12, v[54:55]
	v_ashrrev_i32_e32 v79, 31, v78
	v_lshl_add_u64 v[98:99], s[10:11], 0, v[104:105]
	v_lshl_add_u64 v[98:99], v[98:99], 0, v[78:79]
	v_ashrrev_i32_e32 v77, 31, v76
	v_ashrrev_i32_e32 v75, 31, v74
	s_add_i32 s27, s27, s94
	s_xor_b32 s26, s26, 1
	s_cmpk_lt_i32 s27, 0x400
	s_waitcnt vmcnt(3)
	v_pk_mul_f32 v[66:67], v[12:13], v[66:67]
	s_waitcnt vmcnt(2)
	v_pk_mul_f32 v[62:63], v[8:9], v[62:63]
	s_waitcnt vmcnt(1)
	v_pk_mul_f32 v[58:59], v[4:5], v[58:59]
	s_waitcnt vmcnt(0)
	v_pk_mul_f32 v[72:73], v[0:1], v[72:73]
	v_pk_mul_f32 v[56:57], v[2:3], v[56:57]
	v_cvt_pk_fp8_f32 v120, v72, v73
	v_cvt_pk_fp8_f32 v117, v66, v67
	v_cvt_pk_fp8_f32 v118, v62, v63
	v_cvt_pk_fp8_f32 v119, v58, v59
	v_cvt_pk_fp8_f32 v120, v56, v57 op_sel:[0,0,1]
	v_mul_f32_e32 v56, 0x45800000, v32
	v_cndmask_b32_e64 v32, v32, v56, s[0:1]
	v_pk_mul_f32 v[50:51], v[50:51], v[32:33] op_sel_hi:[1,0]
	v_mov_b32_e32 v56, v33
	v_pk_mul_f32 v[50:51], v[12:13], v[50:51]
	v_pk_mul_f32 v[52:53], v[52:53], v[32:33] op_sel_hi:[1,0]
	v_cvt_pk_fp8_f32 v56, v50, v51
	v_pk_mul_f32 v[52:53], v[14:15], v[52:53]
	v_pk_mul_f32 v[46:47], v[46:47], v[32:33] op_sel_hi:[1,0]
	v_pk_mul_f32 v[42:43], v[42:43], v[32:33] op_sel_hi:[1,0]
	v_cvt_pk_fp8_f32 v56, v52, v53 op_sel:[0,0,1]
	v_pk_mul_f32 v[46:47], v[8:9], v[46:47]
	v_mov_b32_e32 v52, v33
	v_cvt_pk_fp8_f32 v52, v46, v47
	v_pk_mul_f32 v[46:47], v[48:49], v[32:33] op_sel_hi:[1,0]
	v_pk_mul_f32 v[42:43], v[4:5], v[42:43]
	v_pk_mul_f32 v[46:47], v[10:11], v[46:47]
	v_pk_mul_f32 v[68:69], v[14:15], v[68:69]
	v_cvt_pk_fp8_f32 v52, v46, v47 op_sel:[0,0,1]
	v_mov_b32_e32 v46, v33
	v_cvt_pk_fp8_f32 v46, v42, v43
	v_pk_mul_f32 v[42:43], v[44:45], v[32:33] op_sel_hi:[1,0]
	v_pk_mul_f32 v[64:65], v[10:11], v[64:65]
	v_pk_mul_f32 v[42:43], v[6:7], v[42:43]
	v_pk_mul_f32 v[28:29], v[28:29], v[32:33] op_sel_hi:[1,0]
	v_pk_mul_f32 v[60:61], v[6:7], v[60:61]
	v_cvt_pk_fp8_f32 v117, v68, v69 op_sel:[0,0,1]
	v_cvt_pk_fp8_f32 v118, v64, v65 op_sel:[0,0,1]
	v_cvt_pk_fp8_f32 v46, v42, v43 op_sel:[0,0,1]
	v_pk_mul_f32 v[28:29], v[0:1], v[28:29]
	v_mov_b32_e32 v58, v33
	v_cvt_pk_fp8_f32 v119, v60, v61 op_sel:[0,0,1]
	v_cvt_pk_fp8_f32 v58, v28, v29
	v_lshl_add_u64 v[50:51], s[10:11], 0, v[54:55]
	v_lshl_add_u64 v[50:51], v[50:51], 0, v[78:79]
	v_pk_mul_f32 v[28:29], v[30:31], v[32:33] op_sel_hi:[1,0]
	ds_write_b32 v245, v117
	ds_write_b32 v245, v118 offset:16
	ds_write_b32 v245, v119 offset:32
	ds_write_b32 v245, v120 offset:48
	ds_write_b32 v246, v56
	ds_write_b32 v246, v52 offset:16
	ds_write_b32 v246, v46 offset:32
	v_pk_mul_f32 v[28:29], v[2:3], v[28:29]
	s_nop 0
	v_cvt_pk_fp8_f32 v58, v28, v29 op_sel:[0,0,1]
	ds_read2_b32 v[28:29], v116 offset0:32 offset1:48
	ds_read2_b32 v[30:31], v116 offset0:96 offset1:112
	ds_read2_b32 v[42:43], v116 offset0:160 offset1:176
	ds_read2_b32 v[44:45], v116 offset0:224 offset1:240
	ds_read2_b32 v[46:47], v121 offset0:32 offset1:48
	ds_read2_b32 v[48:49], v121 offset0:96 offset1:112
	ds_read2_b32 v[52:53], v121 offset0:160 offset1:176
	ds_read2_b32 v[54:55], v121 offset0:224 offset1:240
	s_waitcnt lgkmcnt(7)
	v_mov_b32_e32 v56, v29
	v_mov_b32_e32 v57, v28
	v_pk_add_f32 v[28:29], v[56:57], 0 op_sel_hi:[1,0]
	s_waitcnt lgkmcnt(6)
	v_mov_b32_e32 v56, v31
	v_mov_b32_e32 v57, v30
	v_pk_add_f32 v[28:29], v[28:29], v[56:57]
	s_waitcnt lgkmcnt(5)
	v_mov_b32_e32 v30, v43
	v_mov_b32_e32 v31, v42
	v_pk_add_f32 v[28:29], v[28:29], v[30:31]
	s_waitcnt lgkmcnt(4)
	v_mov_b32_e32 v30, v45
	v_mov_b32_e32 v31, v44
	v_pk_add_f32 v[28:29], v[28:29], v[30:31]
	s_waitcnt lgkmcnt(3)
	v_mov_b32_e32 v30, v47
	v_mov_b32_e32 v31, v46
	v_pk_add_f32 v[28:29], v[28:29], v[30:31]
	s_waitcnt lgkmcnt(2)
	v_mov_b32_e32 v30, v49
	v_mov_b32_e32 v31, v48
	v_pk_add_f32 v[28:29], v[28:29], v[30:31]
	s_waitcnt lgkmcnt(1)
	v_mov_b32_e32 v30, v53
	v_mov_b32_e32 v31, v52
	v_pk_add_f32 v[28:29], v[28:29], v[30:31]
	s_waitcnt lgkmcnt(0)
	v_mov_b32_e32 v30, v55
	v_mov_b32_e32 v31, v54
	v_pk_add_f32 v[28:29], v[28:29], v[30:31]
	ds_write_b32 v246, v58 offset:48
	v_pk_fma_f32 v[28:29], v[28:29], s[14:15], v[80:81] op_sel_hi:[1,0,0]
	s_nop 0
	v_mul_f32_e32 v30, 0x4b800000, v29
	v_cmp_gt_f32_e64 s[0:1], s12, v29
	s_nop 1
	v_cndmask_b32_e64 v29, v29, v30, s[0:1]
	v_rsq_f32_e32 v29, v29
	v_lshlrev_b64 v[30:31], 12, v[76:77]
	v_lshl_add_u64 v[30:31], s[10:11], 0, v[30:31]
	v_lshl_add_u64 v[30:31], v[30:31], 0, v[78:79]
	v_mul_f32_e32 v32, 0x45800000, v29
	v_cndmask_b32_e64 v32, v29, v32, s[0:1]
	v_pk_mul_f32 v[38:39], v[38:39], v[32:33] op_sel_hi:[1,0]
	v_mov_b32_e32 v29, v33
	v_pk_mul_f32 v[38:39], v[12:13], v[38:39]
	v_pk_mul_f32 v[20:21], v[20:21], v[32:33] op_sel_hi:[1,0]
	v_cvt_pk_fp8_f32 v29, v38, v39
	v_pk_mul_f32 v[38:39], v[40:41], v[32:33] op_sel_hi:[1,0]
	v_pk_mul_f32 v[20:21], v[8:9], v[20:21]
	v_pk_mul_f32 v[38:39], v[14:15], v[38:39]
	v_pk_mul_f32 v[16:17], v[16:17], v[32:33] op_sel_hi:[1,0]
	v_cvt_pk_fp8_f32 v29, v38, v39 op_sel:[0,0,1]
	v_mov_b32_e32 v38, v33
	v_cvt_pk_fp8_f32 v38, v20, v21
	v_pk_mul_f32 v[20:21], v[22:23], v[32:33] op_sel_hi:[1,0]
	v_pk_mul_f32 v[16:17], v[4:5], v[16:17]
	v_pk_mul_f32 v[20:21], v[10:11], v[20:21]
	v_cmp_gt_f32_e64 s[0:1], s12, v28
	v_cvt_pk_fp8_f32 v38, v20, v21 op_sel:[0,0,1]
	v_mov_b32_e32 v20, v33
	v_cvt_pk_fp8_f32 v20, v16, v17
	v_pk_mul_f32 v[16:17], v[24:25], v[32:33] op_sel_hi:[1,0]
	v_mov_b32_e32 v21, v33
	v_pk_mul_f32 v[16:17], v[0:1], v[16:17]
	v_pk_mul_f32 v[18:19], v[18:19], v[32:33] op_sel_hi:[1,0]
	v_cvt_pk_fp8_f32 v21, v16, v17
	v_pk_mul_f32 v[16:17], v[26:27], v[32:33] op_sel_hi:[1,0]
	v_pk_mul_f32 v[18:19], v[6:7], v[18:19]
	v_pk_mul_f32 v[16:17], v[2:3], v[16:17]
	v_cvt_pk_fp8_f32 v20, v18, v19 op_sel:[0,0,1]
	v_cvt_pk_fp8_f32 v21, v16, v17 op_sel:[0,0,1]
	v_mul_f32_e32 v16, 0x4b800000, v28
	v_cndmask_b32_e64 v16, v28, v16, s[0:1]
	v_rsq_f32_e32 v16, v16
	ds_write_b32 v247, v29
	ds_write_b32 v247, v38 offset:16
	ds_write_b32 v247, v20 offset:32
	ds_write_b32 v247, v21 offset:48
	v_lshlrev_b64 v[18:19], 12, v[74:75]
	v_mul_f32_e32 v17, 0x45800000, v16
	v_cndmask_b32_e64 v16, v16, v17, s[0:1]
	v_pk_mul_f32 v[20:21], v[94:95], v[16:17] op_sel_hi:[1,0]
	v_mov_b32_e32 v17, v33
	v_pk_mul_f32 v[12:13], v[12:13], v[20:21]
	s_nop 0
	v_cvt_pk_fp8_f32 v17, v12, v13
	v_lshl_add_u64 v[12:13], s[10:11], 0, v[18:19]
	v_pk_mul_f32 v[18:19], v[90:91], v[16:17] op_sel_hi:[1,0]
	s_nop 0
	v_pk_mul_f32 v[14:15], v[14:15], v[18:19]
	s_nop 0
	v_cvt_pk_fp8_f32 v17, v14, v15 op_sel:[0,0,1]
	s_nop 0
	v_pk_mul_f32 v[14:15], v[92:93], v[16:17] op_sel_hi:[1,0]
	s_nop 0
	v_pk_mul_f32 v[8:9], v[8:9], v[14:15]
	v_mov_b32_e32 v14, v33
	v_cvt_pk_fp8_f32 v14, v8, v9
	v_lshl_add_u64 v[8:9], v[12:13], 0, v[78:79]
	v_pk_mul_f32 v[12:13], v[86:87], v[16:17] op_sel_hi:[1,0]
	s_nop 0
	v_pk_mul_f32 v[10:11], v[10:11], v[12:13]
	v_pk_mul_f32 v[12:13], v[82:83], v[16:17] op_sel_hi:[1,0]
	v_cvt_pk_fp8_f32 v14, v10, v11 op_sel:[0,0,1]
	v_pk_mul_f32 v[10:11], v[88:89], v[16:17] op_sel_hi:[1,0]
	v_pk_mul_f32 v[6:7], v[6:7], v[12:13]
	v_pk_mul_f32 v[4:5], v[4:5], v[10:11]
	v_mov_b32_e32 v10, v33
	v_cvt_pk_fp8_f32 v10, v4, v5
	v_pk_mul_f32 v[4:5], v[84:85], v[16:17] op_sel_hi:[1,0]
	v_cvt_pk_fp8_f32 v10, v6, v7 op_sel:[0,0,1]
	v_pk_mul_f32 v[0:1], v[0:1], v[4:5]
	v_mov_b32_e32 v4, v33
	v_cvt_pk_fp8_f32 v4, v0, v1
	v_pk_mul_f32 v[0:1], v[70:71], v[16:17] op_sel_hi:[1,0]
	s_nop 0
	v_pk_mul_f32 v[0:1], v[2:3], v[0:1]
	s_nop 0
	v_cvt_pk_fp8_f32 v4, v0, v1 op_sel:[0,0,1]
	ds_write_b32 v242, v17
	ds_write_b32 v242, v14 offset:16
	ds_write_b32 v242, v10 offset:32
	ds_write_b32 v242, v4 offset:48
	s_waitcnt lgkmcnt(0)
	ds_read_b128 v[0:3], v243
	ds_read_b128 v[4:7], v243 offset:2560
	ds_read_b128 v[8:11], v243 offset:5120
	ds_read_b128 v[12:15], v243 offset:7680
	s_waitcnt lgkmcnt(3)
	global_store_dwordx4 v244, v[0:3], s[10:11]
	v_add_u32_e32 v244, 0x10000, v244
	s_waitcnt lgkmcnt(2)
	global_store_dwordx4 v244, v[4:7], s[10:11]
	v_add_u32_e32 v244, 0x10000, v244
	s_waitcnt lgkmcnt(1)
	global_store_dwordx4 v244, v[8:11], s[10:11]
	v_add_u32_e32 v244, 0x10000, v244
	s_waitcnt lgkmcnt(0)
	global_store_dwordx4 v244, v[12:15], s[10:11]
	s_nop 1
	s_cbranch_scc0 .LBB0_1276
